# v29 + grid barrier leader rewritten: all CU leaders poll the top-level arrival count directly (no TOPGEN/XGEN hops)
# speedup vs baseline: 1.0036x; 1.0006x over previous
.LBB0_217:
	v_readlane_b32 s0, v253, 45
	v_readlane_b32 s1, v253, 46
	v_mov_b32_e32 v3, 1
	s_waitcnt lgkmcnt(0)
	s_nop 4
	global_atomic_add v3, v129, v3, s[0:1] sc0
	v_cvt_f32_u32_e32 v4, v2
	v_sub_u32_e32 v1, 0, v2
	v_rcp_iflag_f32_e32 v4, v4
	s_nop 1
	v_mul_f32_e32 v4, 0x4f7ffffe, v4
	v_cvt_u32_f32_e32 v4, v4
	v_mul_lo_u32 v1, v1, v4
	v_mul_hi_u32 v1, v4, v1
	v_add_u32_e32 v1, v4, v1
	v_readlane_b32 s0, v253, 49
	v_readlane_b32 s1, v253, 50
	s_waitcnt vmcnt(0)
	v_mul_hi_u32 v1, v3, v1
	v_mul_lo_u32 v4, v1, v2
	v_sub_u32_e32 v4, v3, v4
	v_add_u32_e32 v5, 1, v1
	v_cmp_ge_u32_e32 vcc, v4, v2
	s_nop 1
	v_cndmask_b32_e32 v1, v1, v5, vcc
	v_sub_u32_e32 v5, v4, v2
	v_cndmask_b32_e32 v4, v4, v5, vcc
	v_add_u32_e32 v5, 1, v1
	v_cmp_ge_u32_e32 vcc, v4, v2
	s_nop 1
	v_cndmask_b32_e32 v1, v1, v5, vcc
	v_add_u32_e32 v5, 1, v1
	v_mul_lo_u32 v4, v5, v0
	v_mul_lo_u32 v5, v5, v2
	v_add_u32_e32 v3, 1, v3
	v_cmp_ne_u32_e32 vcc, v3, v5
	s_cbranch_vccnz .Lxb0_poll
	buffer_wbl2 sc1
	s_waitcnt vmcnt(0)
	v_mov_b32_e32 v3, 1
	global_atomic_add v129, v3, s[0:1]
.Lxb0_poll:
	s_mov_b32 s8, 0
.Lxb0_spin:
	global_load_dword v3, v129, s[0:1] sc1
	s_waitcnt vmcnt(0)
	v_cmp_ge_u32_e32 vcc, v3, v4
	s_cbranch_vccnz .Lxb0_done
	s_sleep 1
	s_add_i32 s8, s8, 1
	s_cmp_lt_u32 s8, 0x40000
	s_cbranch_scc1 .Lxb0_spin
.Lxb0_done:
	buffer_inv sc1
	s_waitcnt vmcnt(0)

.LBB0_371:
	v_readlane_b32 s8, v253, 45
	v_readlane_b32 s9, v253, 46
	v_mov_b32_e32 v3, 1
	s_waitcnt lgkmcnt(0)
	s_nop 4
	global_atomic_add v3, v129, v3, s[8:9] sc0
	v_cvt_f32_u32_e32 v4, v2
	v_sub_u32_e32 v1, 0, v2
	v_rcp_iflag_f32_e32 v4, v4
	s_nop 1
	v_mul_f32_e32 v4, 0x4f7ffffe, v4
	v_cvt_u32_f32_e32 v4, v4
	v_mul_lo_u32 v1, v1, v4
	v_mul_hi_u32 v1, v4, v1
	v_add_u32_e32 v1, v4, v1
	v_readlane_b32 s8, v253, 49
	v_readlane_b32 s9, v253, 50
	s_waitcnt vmcnt(0)
	v_mul_hi_u32 v1, v3, v1
	v_mul_lo_u32 v4, v1, v2
	v_sub_u32_e32 v4, v3, v4
	v_add_u32_e32 v5, 1, v1
	v_cmp_ge_u32_e32 vcc, v4, v2
	s_nop 1
	v_cndmask_b32_e32 v1, v1, v5, vcc
	v_sub_u32_e32 v5, v4, v2
	v_cndmask_b32_e32 v4, v4, v5, vcc
	v_add_u32_e32 v5, 1, v1
	v_cmp_ge_u32_e32 vcc, v4, v2
	s_nop 1
	v_cndmask_b32_e32 v1, v1, v5, vcc
	v_add_u32_e32 v5, 1, v1
	v_mul_lo_u32 v4, v5, v0
	v_mul_lo_u32 v5, v5, v2
	v_add_u32_e32 v3, 1, v3
	v_cmp_ne_u32_e32 vcc, v3, v5
	s_cbranch_vccnz .Lxb1_poll
	buffer_wbl2 sc1
	s_waitcnt vmcnt(0)
	v_mov_b32_e32 v3, 1
	global_atomic_add v129, v3, s[8:9]
.Lxb1_poll:
	s_mov_b32 s1, 0
.Lxb1_spin:
	global_load_dword v3, v129, s[8:9] sc1
	s_waitcnt vmcnt(0)
	v_cmp_ge_u32_e32 vcc, v3, v4
	s_cbranch_vccnz .Lxb1_done
	s_sleep 1
	s_add_i32 s1, s1, 1
	s_cmp_lt_u32 s1, 0x40000
	s_cbranch_scc1 .Lxb1_spin
